# w_out GEMM epilogue (x += gate*acc): 32 serialized load-wait-fma-store round trips per tile replaced by a 3-group-deep pipelined version with counted vmcnt (results in place in the accumulators)
# speedup vs baseline: 1.0113x; 1.0027x over previous
.LBB0_477:
	v_lshl_or_b32 v168, s34, 8, v171
	v_ashrrev_i32_e32 v169, 31, v168
	v_lshl_add_u64 v[130:131], v[168:169], 2, s[62:63]
	global_load_dwordx4 v[142:145], v[130:131], off
	global_load_dwordx4 v[138:141], v[130:131], off offset:64
	global_load_dwordx4 v[134:137], v[130:131], off offset:512
	s_nop 0
	global_load_dwordx4 v[130:133], v[130:131], off offset:576
	v_lshl_add_u64 v[250:251], v[148:149], 0, v[168:169]
	v_lshlrev_b64 v[250:251], 2, v[250:251]
	v_lshl_add_u64 v[218:219], s[0:1], 0, v[250:251]
	global_load_dwordx4 v[174:177], v[218:219], off
	global_load_dwordx4 v[178:181], v[218:219], off offset:64
	global_load_dwordx4 v[182:185], v[218:219], off offset:512
	global_load_dwordx4 v[186:189], v[218:219], off offset:576
	v_lshl_add_u64 v[250:251], v[150:151], 0, v[168:169]
	v_lshlrev_b64 v[250:251], 2, v[250:251]
	v_lshl_add_u64 v[218:219], s[0:1], 0, v[250:251]
	global_load_dwordx4 v[190:193], v[218:219], off
	global_load_dwordx4 v[194:197], v[218:219], off offset:64
	global_load_dwordx4 v[198:201], v[218:219], off offset:512
	global_load_dwordx4 v[202:205], v[218:219], off offset:576
	v_lshl_add_u64 v[250:251], v[152:153], 0, v[168:169]
	v_lshlrev_b64 v[250:251], 2, v[250:251]
	v_lshl_add_u64 v[218:219], s[0:1], 0, v[250:251]
	global_load_dwordx4 v[234:237], v[218:219], off
	global_load_dwordx4 v[238:241], v[218:219], off offset:64
	global_load_dwordx4 v[242:245], v[218:219], off offset:512
	global_load_dwordx4 v[246:249], v[218:219], off offset:576
	s_and_b64 vcc, exec, s[38:39]
	s_mov_b32 s34, s24
	s_mov_b32 s74, s40
	s_mov_b64 s[76:77], s[42:43]
	s_waitcnt vmcnt(8)
	v_lshl_add_u64 v[250:251], v[148:149], 0, v[168:169]
	v_lshlrev_b64 v[250:251], 2, v[250:251]
	v_lshl_add_u64 v[226:227], s[50:51], 0, v[250:251]
	v_pk_fma_f32 v[128:129], v[128:129], v[144:145], v[176:177]
	v_pk_fma_f32 v[126:127], v[126:127], v[142:143], v[174:175]
	v_pk_fma_f32 v[124:125], v[124:125], v[140:141], v[180:181]
	v_pk_fma_f32 v[122:123], v[122:123], v[138:139], v[178:179]
	v_pk_fma_f32 v[120:121], v[120:121], v[136:137], v[184:185]
	v_pk_fma_f32 v[118:119], v[118:119], v[134:135], v[182:183]
	v_pk_fma_f32 v[108:109], v[108:109], v[132:133], v[188:189]
	v_pk_fma_f32 v[106:107], v[106:107], v[130:131], v[186:187]
	global_store_dwordx4 v[226:227], v[126:129], off
	global_store_dwordx4 v[226:227], v[122:125], off offset:64
	global_store_dwordx4 v[226:227], v[118:121], off offset:512
	global_store_dwordx4 v[226:227], v[106:109], off offset:576
	v_lshl_add_u64 v[250:251], v[154:155], 0, v[168:169]
	v_lshlrev_b64 v[250:251], 2, v[250:251]
	v_lshl_add_u64 v[218:219], s[0:1], 0, v[250:251]
	global_load_dwordx4 v[174:177], v[218:219], off
	global_load_dwordx4 v[178:181], v[218:219], off offset:64
	global_load_dwordx4 v[182:185], v[218:219], off offset:512
	global_load_dwordx4 v[186:189], v[218:219], off offset:576
	s_waitcnt vmcnt(12)
	v_lshl_add_u64 v[250:251], v[150:151], 0, v[168:169]
	v_lshlrev_b64 v[250:251], 2, v[250:251]
	v_lshl_add_u64 v[226:227], s[50:51], 0, v[250:251]
	v_pk_fma_f32 v[116:117], v[116:117], v[144:145], v[192:193]
	v_pk_fma_f32 v[114:115], v[114:115], v[142:143], v[190:191]
	v_pk_fma_f32 v[112:113], v[112:113], v[140:141], v[196:197]
	v_pk_fma_f32 v[110:111], v[110:111], v[138:139], v[194:195]
	v_pk_fma_f32 v[104:105], v[104:105], v[136:137], v[200:201]
	v_pk_fma_f32 v[102:103], v[102:103], v[134:135], v[198:199]
	v_pk_fma_f32 v[92:93], v[92:93], v[132:133], v[204:205]
	v_pk_fma_f32 v[90:91], v[90:91], v[130:131], v[202:203]
	global_store_dwordx4 v[226:227], v[114:117], off
	global_store_dwordx4 v[226:227], v[110:113], off offset:64
	global_store_dwordx4 v[226:227], v[102:105], off offset:512
	global_store_dwordx4 v[226:227], v[90:93], off offset:576
	v_lshl_add_u64 v[250:251], v[156:157], 0, v[168:169]
	v_lshlrev_b64 v[250:251], 2, v[250:251]
	v_lshl_add_u64 v[218:219], s[0:1], 0, v[250:251]
	global_load_dwordx4 v[190:193], v[218:219], off
	global_load_dwordx4 v[194:197], v[218:219], off offset:64
	global_load_dwordx4 v[198:201], v[218:219], off offset:512
	global_load_dwordx4 v[202:205], v[218:219], off offset:576
	s_waitcnt vmcnt(16)
	v_lshl_add_u64 v[250:251], v[152:153], 0, v[168:169]
	v_lshlrev_b64 v[250:251], 2, v[250:251]
	v_lshl_add_u64 v[226:227], s[50:51], 0, v[250:251]
	v_pk_fma_f32 v[100:101], v[100:101], v[144:145], v[236:237]
	v_pk_fma_f32 v[98:99], v[98:99], v[142:143], v[234:235]
	v_pk_fma_f32 v[96:97], v[96:97], v[140:141], v[240:241]
	v_pk_fma_f32 v[94:95], v[94:95], v[138:139], v[238:239]
	v_pk_fma_f32 v[88:89], v[88:89], v[136:137], v[244:245]
	v_pk_fma_f32 v[86:87], v[86:87], v[134:135], v[242:243]
	v_pk_fma_f32 v[76:77], v[76:77], v[132:133], v[248:249]
	v_pk_fma_f32 v[74:75], v[74:75], v[130:131], v[246:247]
	global_store_dwordx4 v[226:227], v[98:101], off
	global_store_dwordx4 v[226:227], v[94:97], off offset:64
	global_store_dwordx4 v[226:227], v[86:89], off offset:512
	global_store_dwordx4 v[226:227], v[74:77], off offset:576
	v_lshl_add_u64 v[250:251], v[158:159], 0, v[168:169]
	v_lshlrev_b64 v[250:251], 2, v[250:251]
	v_lshl_add_u64 v[218:219], s[0:1], 0, v[250:251]
	global_load_dwordx4 v[234:237], v[218:219], off
	global_load_dwordx4 v[238:241], v[218:219], off offset:64
	global_load_dwordx4 v[242:245], v[218:219], off offset:512
	global_load_dwordx4 v[246:249], v[218:219], off offset:576
	s_waitcnt vmcnt(16)
	v_lshl_add_u64 v[250:251], v[154:155], 0, v[168:169]
	v_lshlrev_b64 v[250:251], 2, v[250:251]
	v_lshl_add_u64 v[226:227], s[50:51], 0, v[250:251]
	v_pk_fma_f32 v[84:85], v[84:85], v[144:145], v[176:177]
	v_pk_fma_f32 v[82:83], v[82:83], v[142:143], v[174:175]
	v_pk_fma_f32 v[80:81], v[80:81], v[140:141], v[180:181]
	v_pk_fma_f32 v[78:79], v[78:79], v[138:139], v[178:179]
	v_pk_fma_f32 v[72:73], v[72:73], v[136:137], v[184:185]
	v_pk_fma_f32 v[70:71], v[70:71], v[134:135], v[182:183]
	v_pk_fma_f32 v[68:69], v[68:69], v[132:133], v[188:189]
	v_pk_fma_f32 v[66:67], v[66:67], v[130:131], v[186:187]
	global_store_dwordx4 v[226:227], v[82:85], off
	global_store_dwordx4 v[226:227], v[78:81], off offset:64
	global_store_dwordx4 v[226:227], v[70:73], off offset:512
	global_store_dwordx4 v[226:227], v[66:69], off offset:576
	v_lshl_add_u64 v[250:251], v[160:161], 0, v[168:169]
	v_lshlrev_b64 v[250:251], 2, v[250:251]
	v_lshl_add_u64 v[218:219], s[0:1], 0, v[250:251]
	global_load_dwordx4 v[174:177], v[218:219], off
	global_load_dwordx4 v[178:181], v[218:219], off offset:64
	global_load_dwordx4 v[182:185], v[218:219], off offset:512
	global_load_dwordx4 v[186:189], v[218:219], off offset:576
	s_waitcnt vmcnt(16)
	v_lshl_add_u64 v[250:251], v[156:157], 0, v[168:169]
	v_lshlrev_b64 v[250:251], 2, v[250:251]
	v_lshl_add_u64 v[226:227], s[50:51], 0, v[250:251]
	v_pk_fma_f32 v[64:65], v[64:65], v[144:145], v[192:193]
	v_pk_fma_f32 v[62:63], v[62:63], v[142:143], v[190:191]
	v_pk_fma_f32 v[60:61], v[60:61], v[140:141], v[196:197]
	v_pk_fma_f32 v[58:59], v[58:59], v[138:139], v[194:195]
	v_pk_fma_f32 v[56:57], v[56:57], v[136:137], v[200:201]
	v_pk_fma_f32 v[54:55], v[54:55], v[134:135], v[198:199]
	v_pk_fma_f32 v[44:45], v[44:45], v[132:133], v[204:205]
	v_pk_fma_f32 v[42:43], v[42:43], v[130:131], v[202:203]
	global_store_dwordx4 v[226:227], v[62:65], off
	global_store_dwordx4 v[226:227], v[58:61], off offset:64
	global_store_dwordx4 v[226:227], v[54:57], off offset:512
	global_store_dwordx4 v[226:227], v[42:45], off offset:576
	v_lshl_add_u64 v[250:251], v[162:163], 0, v[168:169]
	v_lshlrev_b64 v[250:251], 2, v[250:251]
	v_lshl_add_u64 v[218:219], s[0:1], 0, v[250:251]
	global_load_dwordx4 v[190:193], v[218:219], off
	global_load_dwordx4 v[194:197], v[218:219], off offset:64
	global_load_dwordx4 v[198:201], v[218:219], off offset:512
	global_load_dwordx4 v[202:205], v[218:219], off offset:576
	s_waitcnt vmcnt(16)
	v_lshl_add_u64 v[250:251], v[158:159], 0, v[168:169]
	v_lshlrev_b64 v[250:251], 2, v[250:251]
	v_lshl_add_u64 v[226:227], s[50:51], 0, v[250:251]
	v_pk_fma_f32 v[52:53], v[52:53], v[144:145], v[236:237]
	v_pk_fma_f32 v[50:51], v[50:51], v[142:143], v[234:235]
	v_pk_fma_f32 v[48:49], v[48:49], v[140:141], v[240:241]
	v_pk_fma_f32 v[46:47], v[46:47], v[138:139], v[238:239]
	v_pk_fma_f32 v[40:41], v[40:41], v[136:137], v[244:245]
	v_pk_fma_f32 v[38:39], v[38:39], v[134:135], v[242:243]
	v_pk_fma_f32 v[28:29], v[28:29], v[132:133], v[248:249]
	v_pk_fma_f32 v[26:27], v[26:27], v[130:131], v[246:247]
	global_store_dwordx4 v[226:227], v[50:53], off
	global_store_dwordx4 v[226:227], v[46:49], off offset:64
	global_store_dwordx4 v[226:227], v[38:41], off offset:512
	global_store_dwordx4 v[226:227], v[26:29], off offset:576
	s_waitcnt vmcnt(12)
	v_lshl_add_u64 v[250:251], v[160:161], 0, v[168:169]
	v_lshlrev_b64 v[250:251], 2, v[250:251]
	v_lshl_add_u64 v[226:227], s[50:51], 0, v[250:251]
	v_pk_fma_f32 v[36:37], v[36:37], v[144:145], v[176:177]
	v_pk_fma_f32 v[34:35], v[34:35], v[142:143], v[174:175]
	v_pk_fma_f32 v[32:33], v[32:33], v[140:141], v[180:181]
	v_pk_fma_f32 v[30:31], v[30:31], v[138:139], v[178:179]
	v_pk_fma_f32 v[24:25], v[24:25], v[136:137], v[184:185]
	v_pk_fma_f32 v[22:23], v[22:23], v[134:135], v[182:183]
	v_pk_fma_f32 v[12:13], v[12:13], v[132:133], v[188:189]
	v_pk_fma_f32 v[10:11], v[10:11], v[130:131], v[186:187]
	global_store_dwordx4 v[226:227], v[34:37], off
	global_store_dwordx4 v[226:227], v[30:33], off offset:64
	global_store_dwordx4 v[226:227], v[22:25], off offset:512
	global_store_dwordx4 v[226:227], v[10:13], off offset:576
	s_waitcnt vmcnt(8)
	v_lshl_add_u64 v[250:251], v[162:163], 0, v[168:169]
	v_lshlrev_b64 v[250:251], 2, v[250:251]
	v_lshl_add_u64 v[226:227], s[50:51], 0, v[250:251]
	v_pk_fma_f32 v[20:21], v[20:21], v[144:145], v[192:193]
	v_pk_fma_f32 v[18:19], v[18:19], v[142:143], v[190:191]
	v_pk_fma_f32 v[16:17], v[16:17], v[140:141], v[196:197]
	v_pk_fma_f32 v[14:15], v[14:15], v[138:139], v[194:195]
	v_pk_fma_f32 v[8:9], v[8:9], v[136:137], v[200:201]
	v_pk_fma_f32 v[6:7], v[6:7], v[134:135], v[198:199]
	v_pk_fma_f32 v[4:5], v[4:5], v[132:133], v[204:205]
	v_pk_fma_f32 v[2:3], v[2:3], v[130:131], v[202:203]
	global_store_dwordx4 v[226:227], v[18:21], off
	global_store_dwordx4 v[226:227], v[14:17], off offset:64
	global_store_dwordx4 v[226:227], v[6:9], off offset:512
	global_store_dwordx4 v[226:227], v[2:5], off offset:576
	s_mov_b64 s[50:51], s[86:87]
	v_readlane_b32 s86, v255, 33
	v_readlane_b32 s87, v255, 34
	s_cbranch_vccnz .LBB0_486
